# v75 + code placement: 14 hot loop heads (9 GEMM K-loops, fox, dil, P10 tile/emit, P11 pair) pinned to 64-byte boundaries
# baseline (speedup 1.0000x reference)
.LBB0_176:
	s_add_u32 s56, s26, 0x100
	s_addc_u32 s57, s27, 0
	v_mov_b32_e32 v167, v165
	v_mov_b32_e32 v169, v165
	s_add_u32 s58, s28, 0x100
	v_mov_b32_e32 v175, v165
	v_mov_b32_e32 v177, v165
	v_lshl_add_u64 v[178:179], s[16:17], 0, v[168:169]
	v_lshl_add_u64 v[180:181], s[16:17], 0, v[166:167]
	s_addc_u32 s59, s29, 0
	s_mov_b32 s60, -2
	s_mov_b64 s[26:27], 0
	v_add_u32_e32 v252, 0x10000, v204
	v_add_u32_e32 v253, 0x10000, v205
	s_branch .LBB0_178
	.p2alignl 6, 3212836864

.LBB0_286:
	s_lshl_b32 s9, s79, 14
	s_add_i32 s9, s9, 0xc000
	s_and_b32 s43, s9, 0xc000
	v_mad_i64_i32 v[32:33], s[80:81], s8, v234, v[130:131]
	s_add_i32 s9, s43, s57
	s_mov_b32 s80, m0
	s_mov_b32 m0, s9
	s_nop 0
	global_load_lds_dwordx4 v[32:33], off
	s_mov_b32 m0, s80
	v_mad_i64_i32 v[32:33], s[8:9], s8, v234, v[132:133]
	s_add_i32 s8, s43, s58
	s_mov_b32 s9, m0
	s_mov_b32 m0, s8
	s_nop 0
	global_load_lds_dwordx4 v[32:33], off
	s_mov_b32 m0, s9
	.p2alignl 6, 3212836864

.LBB0_331:
	s_cmp_eq_u32 s83, 1
	s_cselect_b32 s0, 3, 15
	s_cselect_b32 s1, 2, 4
	s_cmp_eq_u32 s83, 0
	s_cselect_b32 s84, 0, s1
	s_cselect_b32 s20, 0, s0
	s_lshl_b32 s0, s83, 2
	s_or_b32 s89, s0, s23
	s_lshr_b32 s88, 16, s84
	s_lshl_b32 s8, s89, 7
	s_add_u32 s0, s78, s8
	s_addc_u32 s1, s79, 0
	s_and_b32 s85, s20, s76
	s_add_u32 s20, s80, s8
	v_lshl_add_u64 v[34:35], v[160:161], 0, s[8:9]
	s_addc_u32 s21, s81, 0
	s_sub_i32 s8, s82, s85
	s_ashr_i32 s90, s8, s84
	s_add_i32 s8, s90, 0xffffff80
	v_add_u32_e32 v0, s8, v174
	global_load_dwordx4 v[66:69], v[34:35], off offset:3072
	global_load_dwordx4 v[70:73], v[34:35], off offset:3104
	global_load_dwordx4 v[74:77], v[34:35], off offset:3136
	global_load_dwordx4 v[78:81], v[34:35], off offset:3168
	v_max_i32_e32 v34, 0, v0
	v_lshlrev_b32_e32 v34, s84, v34
	v_max_i32_e32 v38, -16, v0
	v_max_i32_e32 v40, 0xffffffe0, v0
	v_max_i32_e32 v0, 0xffffffd0, v0
	v_add_u32_e32 v34, s85, v34
	v_add_lshl_u32 v38, v38, 16, s84
	v_add_lshl_u32 v40, v40, 32, s84
	v_add_lshl_u32 v0, v0, 48, s84
	v_min_i32_e32 v36, 0x1fff, v34
	v_mov_b64_e32 v[34:35], s[20:21]
	v_add_u32_e32 v38, s85, v38
	v_add_u32_e32 v40, s85, v40
	v_add_u32_e32 v0, s85, v0
	v_mad_i64_i32 v[36:37], s[86:87], v36, s30, v[34:35]
	v_mov_b32_e32 v157, v1
	v_min_i32_e32 v38, 0x1fff, v38
	v_min_i32_e32 v40, 0x1fff, v40
	v_min_i32_e32 v0, 0x1fff, v0
	s_mov_b32 m0, s24
	s_waitcnt lgkmcnt(0)
	v_lshl_add_u64 v[36:37], v[36:37], 0, v[156:157]
	v_mad_i64_i32 v[38:39], s[86:87], v38, s30, v[34:35]
	v_mad_i64_i32 v[40:41], s[86:87], v40, s30, v[34:35]
	v_mad_i64_i32 v[34:35], s[86:87], v0, s30, v[34:35]
	v_add_u32_e32 v0, s90, v178
	global_load_lds_dwordx4 v[36:37], off
	v_lshl_add_u64 v[38:39], v[38:39], 0, v[156:157]
	s_mov_b32 m0, s31
	v_max_i32_e32 v0, 0, v0
	global_load_lds_dwordx4 v[38:39], off
	v_lshl_add_u64 v[40:41], v[40:41], 0, v[156:157]
	s_mov_b32 m0, s33
	v_lshlrev_b32_e32 v0, s84, v0
	global_load_lds_dwordx4 v[40:41], off
	v_lshl_add_u64 v[34:35], v[34:35], 0, v[156:157]
	s_mov_b32 m0, s34
	v_add_u32_e32 v0, s85, v0
	global_load_lds_dwordx4 v[34:35], off
	v_lshl_add_u64 v[36:37], v[36:37], 0, 64
	s_mov_b32 m0, s35
	v_min_u32_e32 v0, 0x1fff, v0
	global_load_lds_dwordx4 v[36:37], off
	v_lshl_add_u64 v[36:37], v[38:39], 0, 64
	s_mov_b32 m0, s36
	v_mul_u32_u24_e32 v0, 0xf00, v0
	global_load_lds_dwordx4 v[36:37], off
	v_lshl_add_u64 v[36:37], v[40:41], 0, 64
	s_mov_b32 m0, s37
	v_lshlrev_b32_e32 v0, 1, v0
	global_load_lds_dwordx4 v[36:37], off
	v_lshl_add_u64 v[36:37], s[0:1], 0, v[0:1]
	v_add_u32_e32 v0, s8, v173
	v_max_i32_e32 v0, 0, v0
	v_lshlrev_b32_e32 v0, s84, v0
	v_add_u32_e32 v0, s85, v0
	v_min_u32_e32 v0, 0x1fff, v0
	v_lshl_add_u64 v[34:35], v[34:35], 0, 64
	s_mov_b32 m0, s38
	v_mul_u32_u24_e32 v0, 0xf00, v0
	global_load_lds_dwordx4 v[34:35], off
	v_lshlrev_b64 v[34:35], 1, v[146:147]
	v_lshlrev_b32_e32 v0, 1, v0
	v_lshl_add_u64 v[36:37], v[36:37], 0, v[34:35]
	v_lshl_add_u64 v[38:39], s[0:1], 0, v[0:1]
	v_lshl_add_u64 v[38:39], v[38:39], 0, v[34:35]
	global_load_dwordx4 v[114:117], v[36:37], off offset:96
	global_load_dwordx4 v[134:137], v[36:37], off offset:64
	global_load_dwordx4 v[130:133], v[38:39], off offset:96
	global_load_dwordx4 v[118:121], v[38:39], off offset:64
	global_load_dwordx4 v[122:125], v[36:37], off offset:32
	global_load_dwordx4 v[142:145], v[36:37], off
	global_load_dwordx4 v[138:141], v[38:39], off offset:32
	global_load_dwordx4 v[126:129], v[38:39], off
	v_subrev_u32_e32 v0, s85, v159
	s_mul_i32 s86, s88, 31
	s_mulk_i32 s89, 0x210
	v_ashrrev_i32_e32 v0, s84, v0
	s_addk_i32 s86, 0xc0
	s_add_i32 s88, s89, 0
	v_add_u32_e32 v0, v175, v0
	s_mov_b32 s87, 2
	s_lshr_b32 s86, s86, 6
	s_add_i32 s88, s88, 0x20000
	v_lshl_add_u64 v[162:163], s[0:1], 0, v[34:35]
	v_lshl_add_u64 v[164:165], s[20:21], 0, v[156:157]
	v_subrev_u32_e32 v157, s90, v0
	.p2alignl 6, 3212836864

.LBB0_429:
	s_add_u32 s60, s24, 0x100
	s_addc_u32 s61, s25, 0
	v_mov_b32_e32 v101, v151
	v_mov_b32_e32 v105, v151
	s_add_u32 s62, s26, 0x100
	v_mov_b32_e32 v0, 0
	v_mov_b32_e32 v117, v151
	v_mov_b32_e32 v119, v151
	v_lshl_add_u64 v[154:155], s[16:17], 0, v[104:105]
	v_lshl_add_u64 v[156:157], s[16:17], 0, v[100:101]
	s_addc_u32 s63, s27, 0
	s_mov_b32 s64, -2
	s_mov_b64 s[24:25], 0
	v_mov_b32_e32 v1, v0
	v_mov_b32_e32 v2, v0
	v_mov_b32_e32 v3, v0
	v_mov_b32_e32 v4, v0
	v_mov_b32_e32 v5, v0
	v_mov_b32_e32 v6, v0
	v_mov_b32_e32 v7, v0
	v_mov_b32_e32 v16, v0
	v_mov_b32_e32 v17, v0
	v_mov_b32_e32 v18, v0
	v_mov_b32_e32 v19, v0
	v_mov_b32_e32 v20, v0
	v_mov_b32_e32 v21, v0
	v_mov_b32_e32 v22, v0
	v_mov_b32_e32 v23, v0
	v_mov_b32_e32 v32, v0
	v_mov_b32_e32 v33, v0
	v_mov_b32_e32 v34, v0
	v_mov_b32_e32 v35, v0
	v_mov_b32_e32 v36, v0
	v_mov_b32_e32 v37, v0
	v_mov_b32_e32 v38, v0
	v_mov_b32_e32 v39, v0
	v_mov_b32_e32 v48, v0
	v_mov_b32_e32 v49, v0
	v_mov_b32_e32 v50, v0
	v_mov_b32_e32 v51, v0
	v_mov_b32_e32 v52, v0
	v_mov_b32_e32 v53, v0
	v_mov_b32_e32 v54, v0
	v_mov_b32_e32 v55, v0
	v_mov_b32_e32 v8, v0
	v_mov_b32_e32 v9, v0
	v_mov_b32_e32 v10, v0
	v_mov_b32_e32 v11, v0
	v_mov_b32_e32 v12, v0
	v_mov_b32_e32 v13, v0
	v_mov_b32_e32 v14, v0
	v_mov_b32_e32 v15, v0
	v_mov_b32_e32 v24, v0
	v_mov_b32_e32 v25, v0
	v_mov_b32_e32 v26, v0
	v_mov_b32_e32 v27, v0
	v_mov_b32_e32 v28, v0
	v_mov_b32_e32 v29, v0
	v_mov_b32_e32 v30, v0
	v_mov_b32_e32 v31, v0
	v_mov_b32_e32 v40, v0
	v_mov_b32_e32 v41, v0
	v_mov_b32_e32 v42, v0
	v_mov_b32_e32 v43, v0
	v_mov_b32_e32 v44, v0
	v_mov_b32_e32 v45, v0
	v_mov_b32_e32 v46, v0
	v_mov_b32_e32 v47, v0
	v_mov_b32_e32 v56, v0
	v_mov_b32_e32 v57, v0
	v_mov_b32_e32 v58, v0
	v_mov_b32_e32 v59, v0
	v_mov_b32_e32 v60, v0
	v_mov_b32_e32 v61, v0
	v_mov_b32_e32 v62, v0
	v_mov_b32_e32 v63, v0
	v_mov_b32_e32 v64, v0
	v_mov_b32_e32 v65, v0
	v_mov_b32_e32 v66, v0
	v_mov_b32_e32 v67, v0
	v_mov_b32_e32 v68, v0
	v_mov_b32_e32 v69, v0
	v_mov_b32_e32 v70, v0
	v_mov_b32_e32 v71, v0
	v_mov_b32_e32 v80, v0
	v_mov_b32_e32 v81, v0
	v_mov_b32_e32 v82, v0
	v_mov_b32_e32 v83, v0
	v_mov_b32_e32 v84, v0
	v_mov_b32_e32 v85, v0
	v_mov_b32_e32 v86, v0
	v_mov_b32_e32 v87, v0
	v_mov_b32_e32 v96, v0
	v_mov_b32_e32 v97, v0
	v_mov_b32_e32 v98, v0
	v_mov_b32_e32 v99, v0
	v_mov_b32_e32 v108, v0
	v_mov_b32_e32 v109, v0
	v_mov_b32_e32 v110, v0
	v_mov_b32_e32 v111, v0
	v_mov_b32_e32 v128, v0
	v_mov_b32_e32 v129, v0
	v_mov_b32_e32 v130, v0
	v_mov_b32_e32 v131, v0
	v_mov_b32_e32 v132, v0
	v_mov_b32_e32 v133, v0
	v_mov_b32_e32 v134, v0
	v_mov_b32_e32 v135, v0
	v_mov_b32_e32 v72, v0
	v_mov_b32_e32 v73, v0
	v_mov_b32_e32 v74, v0
	v_mov_b32_e32 v75, v0
	v_mov_b32_e32 v76, v0
	v_mov_b32_e32 v77, v0
	v_mov_b32_e32 v78, v0
	v_mov_b32_e32 v79, v0
	v_mov_b32_e32 v88, v0
	v_mov_b32_e32 v89, v0
	v_mov_b32_e32 v90, v0
	v_mov_b32_e32 v91, v0
	v_mov_b32_e32 v92, v0
	v_mov_b32_e32 v93, v0
	v_mov_b32_e32 v94, v0
	v_mov_b32_e32 v95, v0
	v_mov_b32_e32 v120, v0
	v_mov_b32_e32 v121, v0
	v_mov_b32_e32 v122, v0
	v_mov_b32_e32 v123, v0
	v_mov_b32_e32 v124, v0
	v_mov_b32_e32 v125, v0
	v_mov_b32_e32 v126, v0
	v_mov_b32_e32 v127, v0
	v_mov_b32_e32 v136, v0
	v_mov_b32_e32 v137, v0
	v_mov_b32_e32 v138, v0
	v_mov_b32_e32 v139, v0
	v_mov_b32_e32 v140, v0
	v_mov_b32_e32 v141, v0
	v_mov_b32_e32 v142, v0
	v_mov_b32_e32 v143, v0
	v_add_u32_e32 v252, 0x10000, v167
	v_add_u32_e32 v253, 0x10000, v168
	s_branch .LBB0_431
	.p2alignl 6, 3212836864

.LBB0_589:
	s_lshl_b32 s4, s80, 10
	s_and_b32 s4, s4, 0x400
	s_add_u32 s27, s38, 0x100
	s_addc_u32 s86, s39, 0
	v_mov_b32_e32 v171, v165
	v_mov_b32_e32 v169, v165
	s_add_u32 s87, s40, 0x100
	v_add_u32_e32 v208, s4, v199
	v_lshl_add_u64 v[174:175], s[18:19], 0, v[168:169]
	v_lshl_add_u64 v[176:177], s[18:19], 0, v[170:171]
	s_addc_u32 s88, s41, 0
	s_mov_b32 s89, -2
	s_mov_b64 s[4:5], 0
	v_add_u32_e32 v252, 0x10000, v197
	v_add_u32_e32 v253, 0x10000, v198
	s_branch .LBB0_591
	.p2alignl 6, 3212836864

.LBB0_671:
	s_add_u32 s27, s34, 0x100
	s_addc_u32 s82, s35, 0
	v_mov_b32_e32 v167, v165
	v_mov_b32_e32 v169, v165
	s_add_u32 s83, s38, 0x100
	v_mov_b32_e32 v175, v165
	v_mov_b32_e32 v177, v165
	v_lshl_add_u64 v[178:179], s[16:17], 0, v[168:169]
	v_lshl_add_u64 v[180:181], s[16:17], 0, v[166:167]
	s_addc_u32 s84, s39, 0
	s_mov_b32 s85, -2
	s_mov_b64 s[34:35], 0
	v_add_u32_e32 v252, 0x10000, v205
	v_add_u32_e32 v253, 0x10000, v206
	s_branch .LBB0_673
	.p2alignl 6, 3212836864

.LBB0_816:
	s_add_u32 s56, s26, 0x100
	s_addc_u32 s57, s27, 0
	v_mov_b32_e32 v169, v165
	v_mov_b32_e32 v171, v165
	s_add_u32 s58, s28, 0x100
	v_mov_b32_e32 v175, v165
	v_mov_b32_e32 v177, v165
	v_lshl_add_u64 v[178:179], s[14:15], 0, v[170:171]
	v_lshl_add_u64 v[180:181], s[14:15], 0, v[168:169]
	s_addc_u32 s59, s29, 0
	s_mov_b32 s60, -2
	s_mov_b64 s[26:27], 0
	v_add_u32_e32 v252, 0x10000, v173
	v_add_u32_e32 v253, 0x10000, v206
	s_branch .LBB0_818
	.p2alignl 6, 3212836864

.LBB0_838:
	s_add_u32 s36, s4, 0x100
	s_addc_u32 s37, s5, 0
	v_mov_b32_e32 v129, v137
	v_mov_b32_e32 v131, v137
	s_add_u32 s57, s6, 0x100
	v_mov_b64_e32 v[0:1], 0
	v_mov_b64_e32 v[2:3], 0
	v_mov_b64_e32 v[4:5], 0
	v_mov_b64_e32 v[6:7], 0
	v_mov_b64_e32 v[8:9], 0
	v_mov_b64_e32 v[10:11], 0
	v_mov_b64_e32 v[12:13], 0
	v_mov_b64_e32 v[14:15], 0
	v_mov_b64_e32 v[16:17], 0
	v_mov_b64_e32 v[18:19], 0
	v_mov_b64_e32 v[20:21], 0
	v_mov_b64_e32 v[22:23], 0
	v_mov_b64_e32 v[24:25], 0
	v_mov_b64_e32 v[26:27], 0
	v_mov_b64_e32 v[28:29], 0
	v_mov_b64_e32 v[30:31], 0
	v_mov_b64_e32 v[32:33], 0
	v_mov_b64_e32 v[34:35], 0
	v_mov_b64_e32 v[36:37], 0
	v_mov_b64_e32 v[38:39], 0
	v_mov_b64_e32 v[40:41], 0
	v_mov_b64_e32 v[42:43], 0
	v_mov_b64_e32 v[44:45], 0
	v_mov_b64_e32 v[46:47], 0
	v_mov_b64_e32 v[48:49], 0
	v_mov_b64_e32 v[50:51], 0
	v_mov_b64_e32 v[52:53], 0
	v_mov_b64_e32 v[54:55], 0
	v_mov_b64_e32 v[56:57], 0
	v_mov_b64_e32 v[58:59], 0
	v_mov_b64_e32 v[60:61], 0
	v_mov_b64_e32 v[62:63], 0
	v_mov_b64_e32 v[64:65], 0
	v_mov_b64_e32 v[66:67], 0
	v_mov_b64_e32 v[68:69], 0
	v_mov_b64_e32 v[70:71], 0
	v_mov_b64_e32 v[72:73], 0
	v_mov_b64_e32 v[74:75], 0
	v_mov_b64_e32 v[76:77], 0
	v_mov_b64_e32 v[78:79], 0
	v_mov_b64_e32 v[80:81], 0
	v_mov_b64_e32 v[82:83], 0
	v_mov_b64_e32 v[84:85], 0
	v_mov_b64_e32 v[86:87], 0
	v_mov_b64_e32 v[88:89], 0
	v_mov_b64_e32 v[90:91], 0
	v_mov_b64_e32 v[92:93], 0
	v_mov_b64_e32 v[94:95], 0
	v_mov_b64_e32 v[96:97], 0
	v_mov_b64_e32 v[98:99], 0
	v_mov_b64_e32 v[100:101], 0
	v_mov_b64_e32 v[102:103], 0
	v_mov_b64_e32 v[104:105], 0
	v_mov_b64_e32 v[106:107], 0
	v_mov_b64_e32 v[108:109], 0
	v_mov_b64_e32 v[110:111], 0
	v_mov_b64_e32 v[112:113], 0
	v_mov_b64_e32 v[114:115], 0
	v_mov_b64_e32 v[116:117], 0
	v_mov_b64_e32 v[118:119], 0
	v_mov_b64_e32 v[120:121], 0
	v_mov_b64_e32 v[122:123], 0
	v_mov_b64_e32 v[124:125], 0
	v_mov_b64_e32 v[126:127], 0
	v_mov_b32_e32 v143, v137
	v_mov_b32_e32 v145, v137
	v_lshl_add_u64 v[146:147], s[22:23], 0, v[130:131]
	v_lshl_add_u64 v[148:149], s[22:23], 0, v[128:129]
	s_addc_u32 s60, s7, 0
	s_mov_b32 s61, -2
	s_mov_b64 s[4:5], 0
	v_add_u32_e32 v252, 0x10000, v159
	v_add_u32_e32 v253, 0x10000, v160
	s_branch .LBB0_840
	.p2alignl 6, 3212836864

.LBB0_1124:
	s_or_b64 exec, exec, s[50:51]
	s_barrier
	global_load_dwordx4 v[102:105], v[148:149], off offset:-4096
	global_load_dwordx4 v[118:121], v[148:149], off offset:-3584
	global_load_dwordx4 v[106:109], v[148:149], off offset:-2048
	global_load_dwordx4 v[98:101], v[148:149], off offset:-1536
	global_load_dwordx4 v[110:113], v[148:149], off
	global_load_dwordx4 v[94:97], v[148:149], off offset:512
	global_load_dwordx4 v[114:117], v[148:149], off offset:2048
	global_load_dwordx4 v[90:93], v[148:149], off offset:2560
	s_waitcnt vmcnt(8)
	v_cvt_f16_f32_e32 v5, v0
	v_cvt_f16_f32_e32 v7, v1
	v_cvt_f16_f32_e32 v12, v2
	v_cvt_f16_f32_e32 v13, v3
	v_cmp_eq_u32_e32 vcc, 0, v6
	v_add_u32_e32 v0, s47, v4
	v_lshl_add_u32 v0, v0, 2, 0
	v_cndmask_b32_e32 v14, 0, v5, vcc
	v_cndmask_b32_e32 v15, 0, v7, vcc
	v_cndmask_b32_e32 v16, 0, v12, vcc
	v_cndmask_b32_e32 v17, 0, v13, vcc
	v_cmp_eq_u32_e32 vcc, 1, v6
	v_add_u32_e32 v1, 0x26100, v0
	v_add_u32_e32 v4, 0x26000, v0
	v_cndmask_b32_e32 v18, 0, v5, vcc
	v_cndmask_b32_e32 v19, 0, v7, vcc
	v_cndmask_b32_e32 v20, 0, v12, vcc
	v_cndmask_b32_e32 v21, 0, v13, vcc
	v_cmp_eq_u32_e32 vcc, 2, v6
	ds_read_b128 v[0:3], v1
	ds_read_b128 v[8:11], v4
	v_cndmask_b32_e32 v22, 0, v5, vcc
	v_cndmask_b32_e32 v23, 0, v7, vcc
	v_cndmask_b32_e32 v24, 0, v12, vcc
	v_cndmask_b32_e32 v25, 0, v13, vcc
	v_cmp_eq_u32_e32 vcc, 3, v6
	v_readlane_b32 s0, v254, 31
	s_waitcnt lgkmcnt(1)
	v_cvt_pk_f16_f32 v189, v0, v1
	v_cndmask_b32_e32 v26, 0, v5, vcc
	v_cndmask_b32_e32 v27, 0, v7, vcc
	v_cndmask_b32_e32 v28, 0, v12, vcc
	v_cndmask_b32_e32 v29, 0, v13, vcc
	v_cmp_eq_u32_e32 vcc, 4, v6
	v_ashrrev_i32_e32 v151, 31, v150
	v_readlane_b32 s1, v254, 32
	v_cndmask_b32_e32 v30, 0, v5, vcc
	v_cndmask_b32_e32 v31, 0, v7, vcc
	v_cndmask_b32_e32 v32, 0, v12, vcc
	v_cndmask_b32_e32 v33, 0, v13, vcc
	v_cmp_eq_u32_e32 vcc, 5, v6
	s_cmp_gt_u32 s75, 38
	s_mov_b32 s24, 0
	v_cndmask_b32_e32 v34, 0, v5, vcc
	v_cndmask_b32_e32 v35, 0, v7, vcc
	v_cndmask_b32_e32 v36, 0, v12, vcc
	v_cndmask_b32_e32 v37, 0, v13, vcc
	v_cmp_eq_u32_e32 vcc, 6, v6
	s_waitcnt lgkmcnt(0)
	v_cvt_pk_f16_f32 v190, v8, v9
	v_cvt_pk_f16_f32 v52, v2, v3
	v_cndmask_b32_e32 v38, 0, v5, vcc
	v_cndmask_b32_e32 v39, 0, v7, vcc
	v_cndmask_b32_e32 v40, 0, v12, vcc
	v_cndmask_b32_e32 v41, 0, v13, vcc
	v_cmp_eq_u32_e32 vcc, 7, v6
	v_cvt_pk_f16_f32 v188, v10, v11
	v_lshl_add_u64 v[154:155], v[150:151], 3, s[0:1]
	v_cndmask_b32_e32 v4, 0, v5, vcc
	v_cndmask_b32_e32 v5, 0, v7, vcc
	v_cndmask_b32_e32 v6, 0, v12, vcc
	v_cndmask_b32_e32 v0, 0, v13, vcc
	s_cselect_b64 s[52:53], -1, 0
	v_pack_b32_f16 v137, v20, v21
	v_pack_b32_f16 v136, v18, v19
	v_pack_b32_f16 v135, v16, v17
	v_pack_b32_f16 v134, v14, v15
	v_pack_b32_f16 v133, v28, v29
	v_pack_b32_f16 v132, v26, v27
	v_pack_b32_f16 v131, v24, v25
	v_pack_b32_f16 v130, v22, v23
	v_pack_b32_f16 v129, v36, v37
	v_pack_b32_f16 v128, v34, v35
	v_pack_b32_f16 v127, v32, v33
	v_pack_b32_f16 v126, v30, v31
	v_pack_b32_f16 v125, v6, v0
	v_pack_b32_f16 v124, v4, v5
	v_pack_b32_f16 v123, v40, v41
	v_pack_b32_f16 v122, v38, v39
	v_mov_b32_e32 v87, v86
	v_mov_b32_e32 v88, v86
	v_mov_b32_e32 v89, v86
	.p2alignl 6, 3212836864

.LBB0_1226:
	v_add_u32_e32 v5, v4, v0
	v_ashrrev_i32_e32 v6, 1, v5
	v_bfe_u32 v5, v5, 16, 1
	v_add_u32_e32 v5, -1, v5
	s_movk_i32 s1, 0x7fff
	v_bitop3_b32 v5, v5, v6, s1 bitop3:0x78
	v_fma_f16 v5, v5, v2, v1
	v_max_f16_e32 v5, 0x6400, v5
	v_min_f16_e32 v5, 0x65ff, v5
	v_and_b32_e32 v5, 0x3ff, v5
	v_cmp_lt_i32_sdwa vcc, v3, v5 src0_sel:DWORD src1_sel:WORD_0
	s_add_i32 s0, s0, -1
	s_cmp_eq_u32 s0, 0
	v_cndmask_b32_e32 v0, v0, v6, vcc
	v_cndmask_b32_e32 v4, v6, v4, vcc
	s_cbranch_scc0 .LBB0_1226
	global_load_dwordx2 v[16:17], v[142:143], off sc1
	global_load_dwordx2 v[14:15], v[142:143], off offset:256 sc1
	v_and_b32_e32 v1, 0x8000, v0
	s_mov_b32 s0, 0xffff
	v_and_b32_e32 v2, 0xffff7fff, v0
	v_bitop3_b32 v0, v0, s0, v185 bitop3:0x6c
	v_cmp_eq_u32_e32 vcc, 0, v1
	v_mov_b32_e32 v52, v53
	v_mov_b32_e32 v54, v53
	v_cndmask_b32_e32 v0, v2, v0, vcc
	v_mov_b32_e32 v55, v53
	v_readlane_b32 s43, v0, 0
	v_readlane_b32 s86, v0, 1
	v_readlane_b32 s47, v0, 2
	v_readlane_b32 s46, v0, 3
	v_readlane_b32 s39, v0, 4
	v_readlane_b32 s38, v0, 5
	v_readlane_b32 s37, v0, 6
	v_readlane_b32 s36, v0, 7
	v_readlane_b32 s35, v0, 8
	v_readlane_b32 s34, v0, 9
	v_readlane_b32 s31, v0, 10
	v_readlane_b32 s30, v0, 11
	v_readlane_b32 s79, v0, 12
	v_readlane_b32 s78, v0, 13
	v_readlane_b32 s29, v0, 14
	v_readlane_b32 s28, v0, 15
	v_mov_b32_e32 v56, v53
	v_mov_b32_e32 v57, v53
	v_mov_b32_e32 v58, v53
	v_mov_b32_e32 v59, v53
	v_mov_b64_e32 v[0:1], v[52:53]
	s_mov_b32 s76, 0
	v_mov_b64_e32 v[12:13], v[144:145]
	v_mov_b32_e32 v18, v138
	v_mov_b32_e32 v19, v180
	v_mov_b64_e32 v[2:3], v[54:55]
	v_mov_b64_e32 v[4:5], v[56:57]
	v_mov_b64_e32 v[6:7], v[58:59]
	s_mov_b32 s73, 0
	s_mov_b32 s84, 0
	s_mov_b32 s85, 0
	s_mov_b32 s24, 0
	s_mov_b32 s25, 0
	s_mov_b32 s26, 0
	s_mov_b32 s27, 0
	.p2alignl 6, 3212836864

.LBB0_1462:
	s_or_b64 exec, exec, s[2:3]
	s_ashr_i32 s19, s18, 31
	s_lshl_b64 s[2:3], s[16:17], 12
	s_add_u32 s44, s24, s2
	s_addc_u32 s45, s25, s3
	v_lshlrev_b32_e32 v0, 8, v163
	v_and_b32_e32 v2, -16, v154
	v_lshl_add_u64 v[8:9], s[44:45], 0, v[0:1]
	v_ashrrev_i32_e32 v3, 31, v2
	v_lshl_add_u64 v[20:21], v[8:9], 0, v[2:3]
	global_load_dwordx4 v[8:11], v[20:21], off nt
	global_load_dwordx4 v[12:15], v[20:21], off offset:64 nt
	global_load_dwordx4 v[16:19], v[20:21], off offset:128 nt
	s_nop 0
	global_load_dwordx4 v[20:23], v[20:21], off offset:192 nt
	s_waitcnt lgkmcnt(0)
	v_or_b32_e32 v0, v6, v4
	v_cmp_ge_i32_e32 vcc, s20, v163
	v_lshl_add_u32 v4, v154, 2, s31
	v_or3_b32 v0, v0, v5, v7
	v_cndmask_b32_e32 v5, 0, v163, vcc
	ds_write_b32 v4, v0
	v_lshl_add_u32 v0, v5, 1, s30
	s_waitcnt lgkmcnt(0)
	ds_read_u16 v0, v0
	s_lshl_b64 s[18:19], s[18:19], 13
	v_lshl_add_u64 v[156:157], s[4:5], 0, v[2:3]
	s_mov_b32 s17, 0
	v_or_b32_e32 v199, 64, v163
	v_mov_b32_e32 v200, 0xff800000
	v_mov_b32_e32 v185, 0
	s_waitcnt vmcnt(3)
	v_cvt_scalef32_pk_bf16_fp8 v66, v8, 1.0
	v_cvt_scalef32_pk_bf16_fp8 v67, v8, 1.0 op_sel:[1,0,0]
	v_cvt_scalef32_pk_bf16_fp8 v68, v9, 1.0
	v_cvt_scalef32_pk_bf16_fp8 v69, v9, 1.0 op_sel:[1,0,0]
	v_or_b32_e32 v4, 16, v163
	v_cmp_ge_i32_e32 vcc, s6, v4
	v_or_b32_e32 v5, 32, v163
	v_cndmask_b32_e32 v4, 0, v4, vcc
	v_cmp_ge_i32_e32 vcc, s6, v5
	v_lshl_add_u32 v4, v4, 1, s30
	v_lshlrev_b32_e32 v6, 2, v164
	v_cndmask_b32_e32 v5, 0, v5, vcc
	v_lshl_add_u32 v5, v5, 1, s30
	v_add_u32_e32 v195, s31, v6
	ds_read_u16 v7, v4
	ds_read_u16 v196, v5
	ds_read_b32 v197, v195
	s_waitcnt lgkmcnt(3)
	v_and_b32_e32 v4, 0xffff, v0
	v_mov_b32_e32 v5, s7
	v_lshl_add_u64 v[4:5], s[18:19], 0, v[4:5]
	v_lshlrev_b64 v[4:5], 8, v[4:5]
	v_lshl_add_u64 v[4:5], s[4:5], 0, v[4:5]
	v_lshl_add_u64 v[4:5], v[4:5], 0, v[2:3]
	global_load_dwordx4 v[110:113], v[4:5], off
	global_load_dwordx4 v[106:109], v[4:5], off offset:64
	global_load_dwordx4 v[102:105], v[4:5], off offset:128
	global_load_dwordx4 v[98:101], v[4:5], off offset:192
	s_waitcnt lgkmcnt(2)
	v_and_b32_e32 v4, 0xffff, v7
	v_mov_b32_e32 v5, s7
	v_lshl_add_u64 v[4:5], s[18:19], 0, v[4:5]
	v_lshlrev_b64 v[4:5], 8, v[4:5]
	v_lshl_add_u64 v[4:5], s[4:5], 0, v[4:5]
	v_lshl_add_u64 v[4:5], v[4:5], 0, v[2:3]
	global_load_dwordx4 v[244:247], v[4:5], off
	global_load_dwordx4 v[240:243], v[4:5], off offset:64
	global_load_dwordx4 v[236:239], v[4:5], off offset:128
	global_load_dwordx4 v[232:235], v[4:5], off offset:192
	v_cvt_scalef32_pk_bf16_fp8 v82, v10, 1.0
	v_cvt_scalef32_pk_bf16_fp8 v83, v10, 1.0 op_sel:[1,0,0]
	v_cvt_scalef32_pk_bf16_fp8 v84, v11, 1.0
	v_cvt_scalef32_pk_bf16_fp8 v85, v11, 1.0 op_sel:[1,0,0]
	s_waitcnt vmcnt(10)
	v_cvt_scalef32_pk_bf16_fp8 v70, v12, 1.0
	v_cvt_scalef32_pk_bf16_fp8 v71, v12, 1.0 op_sel:[1,0,0]
	v_cvt_scalef32_pk_bf16_fp8 v72, v13, 1.0
	v_cvt_scalef32_pk_bf16_fp8 v73, v13, 1.0 op_sel:[1,0,0]
	v_cvt_scalef32_pk_bf16_fp8 v86, v14, 1.0
	v_cvt_scalef32_pk_bf16_fp8 v87, v14, 1.0 op_sel:[1,0,0]
	v_cvt_scalef32_pk_bf16_fp8 v88, v15, 1.0
	v_cvt_scalef32_pk_bf16_fp8 v89, v15, 1.0 op_sel:[1,0,0]
	s_waitcnt vmcnt(9)
	v_cvt_scalef32_pk_bf16_fp8 v74, v16, 1.0
	v_cvt_scalef32_pk_bf16_fp8 v75, v16, 1.0 op_sel:[1,0,0]
	v_cvt_scalef32_pk_bf16_fp8 v76, v17, 1.0
	v_cvt_scalef32_pk_bf16_fp8 v77, v17, 1.0 op_sel:[1,0,0]
	v_cvt_scalef32_pk_bf16_fp8 v90, v18, 1.0
	v_cvt_scalef32_pk_bf16_fp8 v91, v18, 1.0 op_sel:[1,0,0]
	v_cvt_scalef32_pk_bf16_fp8 v92, v19, 1.0
	v_cvt_scalef32_pk_bf16_fp8 v93, v19, 1.0 op_sel:[1,0,0]
	s_waitcnt vmcnt(8)
	v_cvt_scalef32_pk_bf16_fp8 v78, v20, 1.0
	v_cvt_scalef32_pk_bf16_fp8 v79, v20, 1.0 op_sel:[1,0,0]
	v_cvt_scalef32_pk_bf16_fp8 v80, v21, 1.0
	v_cvt_scalef32_pk_bf16_fp8 v81, v21, 1.0 op_sel:[1,0,0]
	v_cvt_scalef32_pk_bf16_fp8 v94, v22, 1.0
	v_cvt_scalef32_pk_bf16_fp8 v95, v22, 1.0 op_sel:[1,0,0]
	v_cvt_scalef32_pk_bf16_fp8 v96, v23, 1.0
	v_cvt_pk_f32_fp8_sdwa v[22:23], v23 src0_sel:WORD_1
	v_mov_b32_e32 v2, v1
	v_mov_b32_e32 v3, v1
	v_cvt_pk_bf16_f32 v97, v22, v23
	v_add_u32_e32 v198, s37, v6
	v_mov_b32_e32 v0, v1
	v_mov_b64_e32 v[64:65], v[2:3]
	v_mov_b64_e32 v[60:61], v[2:3]
	v_mov_b64_e32 v[56:57], v[2:3]
	v_mov_b64_e32 v[52:53], v[2:3]
	v_mov_b64_e32 v[48:49], v[2:3]
	v_mov_b64_e32 v[44:45], v[2:3]
	v_mov_b64_e32 v[40:41], v[2:3]
	v_mov_b64_e32 v[36:37], v[2:3]
	v_mov_b64_e32 v[32:33], v[2:3]
	v_mov_b64_e32 v[28:29], v[2:3]
	v_mov_b64_e32 v[24:25], v[2:3]
	v_mov_b64_e32 v[20:21], v[2:3]
	v_mov_b64_e32 v[16:17], v[2:3]
	v_mov_b64_e32 v[12:13], v[2:3]
	v_mov_b64_e32 v[8:9], v[2:3]
	v_mov_b64_e32 v[62:63], v[0:1]
	v_mov_b64_e32 v[58:59], v[0:1]
	v_mov_b64_e32 v[54:55], v[0:1]
	v_mov_b64_e32 v[50:51], v[0:1]
	v_mov_b64_e32 v[46:47], v[0:1]
	v_mov_b64_e32 v[42:43], v[0:1]
	v_mov_b64_e32 v[38:39], v[0:1]
	v_mov_b64_e32 v[34:35], v[0:1]
	v_mov_b64_e32 v[30:31], v[0:1]
	v_mov_b64_e32 v[26:27], v[0:1]
	v_mov_b64_e32 v[22:23], v[0:1]
	v_mov_b64_e32 v[18:19], v[0:1]
	v_mov_b64_e32 v[14:15], v[0:1]
	v_mov_b64_e32 v[10:11], v[0:1]
	v_mov_b64_e32 v[6:7], v[0:1]
	v_mov_b64_e32 v[4:5], v[2:3]
	v_mov_b64_e32 v[2:3], v[0:1]
	.p2alignl 6, 3212836864

.LBB0_1548:
	s_add_u32 s58, s24, 0x100
	s_addc_u32 s59, s25, 0
	v_mov_b32_e32 v169, v165
	v_mov_b32_e32 v171, v165
	s_add_u32 s60, s26, 0x100
	v_mov_b32_e32 v175, v165
	v_mov_b32_e32 v177, v165
	v_lshl_add_u64 v[178:179], s[14:15], 0, v[170:171]
	v_lshl_add_u64 v[180:181], s[14:15], 0, v[168:169]
	s_addc_u32 s61, s27, 0
	s_mov_b32 s62, -2
	s_mov_b64 s[24:25], 0
	s_waitcnt vmcnt(0)
	v_add_u32_e32 v252, 0x10000, v204
	v_add_u32_e32 v253, 0x10000, v205
	s_branch .LBB0_1550
	.p2alignl 6, 3212836864
